# d3 + phase B mixers (sgu / pool / attn MFMA stages): serial ds_read -> wait -> mfma triples regrouped into batches of up to 8 LDS reads in flight with counted lgkmcnt waits
# speedup vs baseline: 1.0022x; 1.0002x over previous
.LBB0_808:
	ds_read_b128 v[188:191], v119
	ds_read_b128 v[192:195], v120
	ds_read_b128 v[204:207], v121
	ds_read_b128 v[208:211], v122
	ds_read_b128 v[212:215], v123
	ds_read_b128 v[226:229], v124
	ds_read_b128 v[230:233], v125
	ds_read_b128 v[234:237], v126
	s_waitcnt lgkmcnt(7)
	v_mfma_f32_16x16x32_bf16 v[44:47], v[188:191], v[12:15], v[44:47]
	s_waitcnt lgkmcnt(6)
	v_mfma_f32_16x16x32_bf16 v[40:43], v[192:195], v[12:15], v[40:43]
	s_waitcnt lgkmcnt(5)
	v_mfma_f32_16x16x32_bf16 v[36:39], v[204:207], v[12:15], v[36:39]
	s_waitcnt lgkmcnt(4)
	v_mfma_f32_16x16x32_bf16 v[32:35], v[208:211], v[12:15], v[32:35]
	s_waitcnt lgkmcnt(3)
	v_mfma_f32_16x16x32_bf16 v[28:31], v[212:215], v[12:15], v[28:31]
	s_waitcnt lgkmcnt(2)
	v_mfma_f32_16x16x32_bf16 v[24:27], v[226:229], v[12:15], v[24:27]
	s_waitcnt lgkmcnt(1)
	v_mfma_f32_16x16x32_bf16 v[20:23], v[230:233], v[12:15], v[20:23]
	s_waitcnt lgkmcnt(0)
	v_mfma_f32_16x16x32_bf16 v[16:19], v[234:237], v[12:15], v[16:19]
.LBB0_809:
	s_andn2_b64 vcc, exec, s[16:17]
	s_cbranch_vccnz .LBB0_811
	ds_read_b128 v[188:191], v127
	ds_read_b128 v[192:195], v128
	ds_read_b128 v[204:207], v129
	ds_read_b128 v[208:211], v130
	ds_read_b128 v[212:215], v131
	ds_read_b128 v[226:229], v132
	ds_read_b128 v[230:233], v133
	ds_read_b128 v[234:237], v134
	s_waitcnt lgkmcnt(7)
	v_mfma_f32_16x16x32_bf16 v[44:47], v[188:191], v[8:11], v[44:47]
	s_waitcnt lgkmcnt(6)
	v_mfma_f32_16x16x32_bf16 v[40:43], v[192:195], v[8:11], v[40:43]
	s_waitcnt lgkmcnt(5)
	v_mfma_f32_16x16x32_bf16 v[36:39], v[204:207], v[8:11], v[36:39]
	s_waitcnt lgkmcnt(4)
	v_mfma_f32_16x16x32_bf16 v[32:35], v[208:211], v[8:11], v[32:35]
	s_waitcnt lgkmcnt(3)
	v_mfma_f32_16x16x32_bf16 v[28:31], v[212:215], v[8:11], v[28:31]
	s_waitcnt lgkmcnt(2)
	v_mfma_f32_16x16x32_bf16 v[24:27], v[226:229], v[8:11], v[24:27]
	s_waitcnt lgkmcnt(1)
	v_mfma_f32_16x16x32_bf16 v[20:23], v[230:233], v[8:11], v[20:23]
	s_waitcnt lgkmcnt(0)
	v_mfma_f32_16x16x32_bf16 v[16:19], v[234:237], v[8:11], v[16:19]
	s_andn2_b64 vcc, exec, s[18:19]
	s_cbranch_vccnz .LBB0_804
	s_branch .LBB0_812

.LBB0_812:
	ds_read_b128 v[188:191], v135
	ds_read_b128 v[192:195], v136
	ds_read_b128 v[204:207], v137
	ds_read_b128 v[208:211], v138
	ds_read_b128 v[212:215], v139
	ds_read_b128 v[226:229], v140
	ds_read_b128 v[230:233], v141
	ds_read_b128 v[234:237], v142
	s_waitcnt lgkmcnt(7)
	v_mfma_f32_16x16x32_bf16 v[44:47], v[188:191], v[4:7], v[44:47]
	s_waitcnt lgkmcnt(6)
	v_mfma_f32_16x16x32_bf16 v[40:43], v[192:195], v[4:7], v[40:43]
	s_waitcnt lgkmcnt(5)
	v_mfma_f32_16x16x32_bf16 v[36:39], v[204:207], v[4:7], v[36:39]
	s_waitcnt lgkmcnt(4)
	v_mfma_f32_16x16x32_bf16 v[32:35], v[208:211], v[4:7], v[32:35]
	s_waitcnt lgkmcnt(3)
	v_mfma_f32_16x16x32_bf16 v[28:31], v[212:215], v[4:7], v[28:31]
	s_waitcnt lgkmcnt(2)
	v_mfma_f32_16x16x32_bf16 v[24:27], v[226:229], v[4:7], v[24:27]
	s_waitcnt lgkmcnt(1)
	v_mfma_f32_16x16x32_bf16 v[20:23], v[230:233], v[4:7], v[20:23]
	s_waitcnt lgkmcnt(0)
	v_mfma_f32_16x16x32_bf16 v[16:19], v[234:237], v[4:7], v[16:19]
	s_branch .LBB0_804

.LBB0_814:
	s_or_b64 exec, exec, s[14:15]
	v_add_u32_e32 v51, v45, v49
	s_waitcnt lgkmcnt(0)
	s_barrier
	ds_read_b128 v[76:79], v51
	ds_read_b128 v[80:83], v51 offset:4096
	ds_read_b128 v[84:87], v51 offset:8192
	ds_read_b128 v[90:93], v51 offset:12288
	ds_read_b128 v[112:115], v51 offset:16384
	ds_read_b128 v[116:119], v51 offset:20480
	ds_read_b128 v[120:123], v51 offset:24576
	ds_read_b128 v[124:127], v51 offset:28672
	ds_read_b128 v[72:75], v89 offset:39168
	v_add_u32_e32 v51, v45, v96
	ds_read_b128 v[128:131], v51
	s_waitcnt lgkmcnt(1)
	v_mfma_f32_16x16x32_bf16 v[76:79], v[76:79], v[72:75], 0
	v_add_u32_e32 v94, s27, v48
	v_ashrrev_i32_e32 v95, 31, v94
	v_lshlrev_b64 v[94:95], 12, v[94:95]
	v_mfma_f32_16x16x32_bf16 v[80:83], v[80:83], v[72:75], 0
	v_lshl_add_u64 v[94:95], s[6:7], 0, v[94:95]
	v_lshl_add_u64 v[56:57], v[56:57], 1, v[94:95]
	s_mov_b64 s[14:15], 0x40e00400
	v_mfma_f32_16x16x32_bf16 v[84:87], v[84:87], v[72:75], 0
	s_add_i32 s26, s26, s75
	s_cmpk_gt_i32 s26, 0xff
	v_mfma_f32_16x16x32_bf16 v[90:93], v[90:93], v[72:75], 0
	v_mfma_f32_16x16x32_bf16 v[112:115], v[112:115], v[72:75], 0
	v_mfma_f32_16x16x32_bf16 v[116:119], v[116:119], v[72:75], 0
	v_mfma_f32_16x16x32_bf16 v[120:123], v[120:123], v[72:75], 0
	v_mfma_f32_16x16x32_bf16 v[72:75], v[124:127], v[72:75], 0
	ds_read_b128 v[124:127], v89 offset:39232
	s_waitcnt lgkmcnt(0)
	v_mfma_f32_16x16x32_bf16 v[76:79], v[128:131], v[124:127], v[76:79]
	ds_read_b128 v[128:131], v51 offset:4096
	s_waitcnt lgkmcnt(0)
	v_mfma_f32_16x16x32_bf16 v[80:83], v[128:131], v[124:127], v[80:83]
	ds_read_b128 v[128:131], v51 offset:8192
	s_waitcnt lgkmcnt(0)
	v_mfma_f32_16x16x32_bf16 v[84:87], v[128:131], v[124:127], v[84:87]
	ds_read_b128 v[128:131], v51 offset:12288
	s_waitcnt lgkmcnt(0)
	v_mfma_f32_16x16x32_bf16 v[90:93], v[128:131], v[124:127], v[90:93]
	ds_read_b128 v[128:131], v51 offset:16384
	s_waitcnt lgkmcnt(0)
	v_mfma_f32_16x16x32_bf16 v[112:115], v[128:131], v[124:127], v[112:115]
	ds_read_b128 v[128:131], v51 offset:20480
	s_waitcnt lgkmcnt(0)
	v_mfma_f32_16x16x32_bf16 v[116:119], v[128:131], v[124:127], v[116:119]
	ds_read_b128 v[128:131], v51 offset:24576
	s_waitcnt lgkmcnt(0)
	v_mfma_f32_16x16x32_bf16 v[120:123], v[128:131], v[124:127], v[120:123]
	ds_read_b128 v[128:131], v51 offset:28672
	v_add_u32_e32 v51, v45, v97
	s_waitcnt lgkmcnt(0)
	v_mfma_f32_16x16x32_bf16 v[72:75], v[128:131], v[124:127], v[72:75]
	ds_read_b128 v[124:127], v89 offset:39296
	ds_read_b128 v[188:191], v51
	ds_read_b128 v[192:195], v51 offset:4096
	ds_read_b128 v[204:207], v51 offset:8192
	ds_read_b128 v[208:211], v51 offset:12288
	ds_read_b128 v[212:215], v51 offset:16384
	ds_read_b128 v[226:229], v51 offset:20480
	ds_read_b128 v[230:233], v51 offset:24576
	s_waitcnt lgkmcnt(6)
	v_mfma_f32_16x16x32_bf16 v[76:79], v[188:191], v[124:127], v[76:79]
	s_waitcnt lgkmcnt(5)
	v_mfma_f32_16x16x32_bf16 v[80:83], v[192:195], v[124:127], v[80:83]
	s_waitcnt lgkmcnt(4)
	v_mfma_f32_16x16x32_bf16 v[84:87], v[204:207], v[124:127], v[84:87]
	s_waitcnt lgkmcnt(3)
	v_mfma_f32_16x16x32_bf16 v[90:93], v[208:211], v[124:127], v[90:93]
	s_waitcnt lgkmcnt(2)
	v_mfma_f32_16x16x32_bf16 v[112:115], v[212:215], v[124:127], v[112:115]
	s_waitcnt lgkmcnt(1)
	v_mfma_f32_16x16x32_bf16 v[116:119], v[226:229], v[124:127], v[116:119]
	s_waitcnt lgkmcnt(0)
	v_mfma_f32_16x16x32_bf16 v[120:123], v[230:233], v[124:127], v[120:123]
	ds_read_b128 v[128:131], v51 offset:28672
	v_add_u32_e32 v51, v45, v98
	s_waitcnt lgkmcnt(0)
	v_mfma_f32_16x16x32_bf16 v[72:75], v[128:131], v[124:127], v[72:75]
	ds_read_b128 v[124:127], v89 offset:39360
	ds_read_b128 v[128:131], v51
	s_waitcnt lgkmcnt(0)
	v_mfma_f32_16x16x32_bf16 v[76:79], v[128:131], v[124:127], v[76:79]
	ds_read_b128 v[128:131], v51 offset:4096
	s_waitcnt vmcnt(7)
	s_nop 5
	v_mul_f32_e32 v32, v32, v76
	s_waitcnt lgkmcnt(0)
	v_mfma_f32_16x16x32_bf16 v[80:83], v[128:131], v[124:127], v[80:83]
	ds_read_b128 v[128:131], v51 offset:8192
	v_mul_f32_e32 v33, v33, v77
	s_waitcnt vmcnt(6)
	s_nop 4
	v_mul_f32_e32 v28, v28, v80
	s_waitcnt lgkmcnt(0)
	v_mfma_f32_16x16x32_bf16 v[84:87], v[128:131], v[124:127], v[84:87]
	ds_read_b128 v[128:131], v51 offset:12288
	v_mul_f32_e32 v29, v29, v81
	s_waitcnt vmcnt(5)
	s_nop 4
	v_mul_f32_e32 v24, v24, v84
	s_waitcnt lgkmcnt(0)
	v_mfma_f32_16x16x32_bf16 v[90:93], v[128:131], v[124:127], v[90:93]
	ds_read_b128 v[128:131], v51 offset:16384
	v_mul_f32_e32 v25, v25, v85
	s_waitcnt vmcnt(4)
	s_nop 4
	v_mul_f32_e32 v20, v20, v90
	s_waitcnt lgkmcnt(0)
	v_mfma_f32_16x16x32_bf16 v[112:115], v[128:131], v[124:127], v[112:115]
	ds_read_b128 v[128:131], v51 offset:20480
	v_mul_f32_e32 v21, v21, v91
	s_waitcnt vmcnt(3)
	s_nop 4
	v_mul_f32_e32 v16, v16, v112
	s_waitcnt lgkmcnt(0)
	v_mfma_f32_16x16x32_bf16 v[116:119], v[128:131], v[124:127], v[116:119]
	ds_read_b128 v[128:131], v51 offset:24576
	v_mul_f32_e32 v17, v17, v113
	s_waitcnt vmcnt(2)
	s_nop 4
	v_mul_f32_e32 v12, v12, v116
	s_waitcnt lgkmcnt(0)
	v_mfma_f32_16x16x32_bf16 v[120:123], v[128:131], v[124:127], v[120:123]
	ds_read_b128 v[128:131], v51 offset:28672
	v_mov_b32_e32 v51, v3
	v_lshl_add_u64 v[56:57], v[56:57], 0, v[50:51]
	v_cvt_pk_bf16_f32 v32, v32, v33
	v_mul_f32_e32 v33, v34, v78
	v_mul_f32_e32 v34, v35, v79
	v_cvt_pk_bf16_f32 v33, v33, v34
	v_add_co_u32_e32 v34, vcc, s90, v56
	v_lshl_add_u64 v[94:95], v[56:57], 0, s[14:15]
	s_nop 0
	v_addc_co_u32_e32 v35, vcc, 0, v57, vcc
	global_store_dwordx2 v[34:35], v[32:33], off offset:1024
	v_cvt_pk_bf16_f32 v28, v28, v29
	v_mul_f32_e32 v29, v30, v82
	s_waitcnt lgkmcnt(0)
	v_mfma_f32_16x16x32_bf16 v[72:75], v[128:131], v[124:127], v[72:75]
	v_mul_f32_e32 v30, v31, v83
	v_cvt_pk_bf16_f32 v29, v29, v30
	global_store_dwordx2 v[94:95], v[28:29], off offset:32
	v_cvt_pk_bf16_f32 v24, v24, v25
	v_mul_f32_e32 v25, v26, v86
	v_mul_f32_e32 v26, v27, v87
	v_cvt_pk_bf16_f32 v25, v25, v26
	global_store_dwordx2 v[94:95], v[24:25], off offset:64
	v_cvt_pk_bf16_f32 v20, v20, v21
	v_mul_f32_e32 v21, v22, v92
	v_mul_f32_e32 v22, v23, v93
	v_cvt_pk_bf16_f32 v21, v21, v22
	global_store_dwordx2 v[94:95], v[20:21], off offset:96
	v_cvt_pk_bf16_f32 v16, v16, v17
	v_mul_f32_e32 v17, v18, v114
	v_mul_f32_e32 v13, v13, v117
	v_mul_f32_e32 v18, v19, v115
	v_cvt_pk_bf16_f32 v17, v17, v18
	global_store_dwordx2 v[94:95], v[16:17], off offset:128
	v_cvt_pk_bf16_f32 v12, v12, v13
	v_mul_f32_e32 v13, v14, v118
	s_waitcnt vmcnt(6)
	v_mul_f32_e32 v8, v8, v120
	v_mul_f32_e32 v9, v9, v121
	v_mul_f32_e32 v14, v15, v119
	v_cvt_pk_bf16_f32 v13, v13, v14
	global_store_dwordx2 v[94:95], v[12:13], off offset:160
	v_cvt_pk_bf16_f32 v8, v8, v9
	v_mul_f32_e32 v9, v10, v122
	s_waitcnt vmcnt(6)
	v_mul_f32_e32 v4, v4, v72
	v_mul_f32_e32 v5, v5, v73
	v_mul_f32_e32 v10, v11, v123
	v_cvt_pk_bf16_f32 v9, v9, v10
	global_store_dwordx2 v[94:95], v[8:9], off offset:192
	v_cvt_pk_bf16_f32 v4, v4, v5
	v_mul_f32_e32 v5, v6, v74
	v_mul_f32_e32 v6, v7, v75
	v_cvt_pk_bf16_f32 v5, v5, v6
	global_store_dwordx2 v[94:95], v[4:5], off offset:224
	s_barrier
	s_cbranch_scc1 .LBB0_828

.LBB0_839:
	s_ashr_i32 s2, s85, 31
	s_ashr_i32 s13, s85, 2
	s_lshr_b32 s2, s2, 28
	s_add_i32 s2, s13, s2
	s_lshl_b32 s2, s2, 4
	s_and_b32 s2, s2, 0xffffff00
	s_ashr_i32 s3, s2, 31
	s_lshl_b64 s[14:15], s[2:3], 12
	s_add_u32 s14, s4, s14
	s_addc_u32 s15, s5, s15
	s_and_b32 s16, s11, 0x180
	s_lshl_b32 s46, s16, 1
	s_add_u32 s14, s14, s46
	s_addc_u32 s15, s15, 0
	s_or_b32 s16, s16, s8
	s_ashr_i32 s17, s16, 31
	s_lshl_b64 s[16:17], s[16:17], 11
	s_add_u32 s16, s9, s16
	s_addc_u32 s17, s10, s17
	s_lshl_b64 s[2:3], s[2:3], 1
	s_add_u32 s2, s16, s2
	s_addc_u32 s3, s17, s3
	v_lshl_add_u64 v[138:139], s[14:15], 0, v[2:3]
	v_mov_b32_e32 v55, v3
	v_lshl_add_u64 v[142:143], s[2:3], 0, v[54:55]
	v_lshl_add_u64 v[4:5], v[138:139], 0, v[40:41]
	global_load_dwordx4 v[4:7], v[4:5], off
	v_lshl_add_u64 v[8:9], v[142:143], 0, v[42:43]
	global_load_dwordx4 v[8:11], v[8:9], off
	v_lshl_add_u64 v[12:13], v[138:139], 0, v[44:45]
	global_load_dwordx4 v[12:15], v[12:13], off
	v_lshl_add_u64 v[16:17], v[142:143], 0, v[46:47]
	global_load_dwordx4 v[16:19], v[16:17], off
	v_lshl_add_u64 v[20:21], v[138:139], 0, v[56:57]
	global_load_dwordx4 v[20:23], v[20:21], off
	v_lshl_add_u64 v[24:25], v[142:143], 0, v[58:59]
	global_load_dwordx4 v[24:27], v[24:25], off
	v_lshl_add_u64 v[28:29], v[138:139], 0, v[60:61]
	global_load_dwordx4 v[28:31], v[28:29], off
	v_lshl_add_u64 v[32:33], v[142:143], 0, v[62:63]
	global_load_dwordx4 v[32:35], v[32:33], off
	v_lshl_add_u64 v[36:37], v[138:139], 0, v[64:65]
	global_load_dwordx4 v[36:39], v[36:37], off
	v_lshl_add_u64 v[80:81], v[142:143], 0, v[66:67]
	global_load_dwordx4 v[80:83], v[80:81], off
	v_lshl_add_u64 v[122:123], v[138:139], 0, v[68:69]
	global_load_dwordx4 v[122:125], v[122:123], off
	v_lshl_add_u64 v[126:127], v[142:143], 0, v[70:71]
	global_load_dwordx4 v[126:129], v[126:127], off
	v_lshl_add_u64 v[130:131], v[138:139], 0, v[72:73]
	global_load_dwordx4 v[130:133], v[130:131], off
	v_lshl_add_u64 v[134:135], v[142:143], 0, v[74:75]
	global_load_dwordx4 v[134:137], v[134:135], off
	v_lshl_add_u64 v[138:139], v[138:139], 0, v[76:77]
	global_load_dwordx4 v[138:141], v[138:139], off
	v_lshl_add_u64 v[142:143], v[142:143], 0, v[78:79]
	global_load_dwordx4 v[142:145], v[142:143], off
	v_mov_b32_e32 v53, v3
	v_add_u32_e32 v51, v1, v49
	s_add_i32 s85, s85, s75
	s_add_i32 s11, s11, s12
	s_cmpk_gt_i32 s85, 0xff
	s_waitcnt vmcnt(15)
	ds_write_b128 v86, v[4:7]
	s_waitcnt vmcnt(14)
	ds_write_b128 v87, v[8:11]
	s_waitcnt vmcnt(13)
	ds_write_b128 v88, v[12:15]
	s_waitcnt vmcnt(12)
	ds_write_b128 v89, v[16:19]
	s_waitcnt vmcnt(11)
	ds_write_b128 v90, v[20:23]
	s_waitcnt vmcnt(10)
	ds_write_b128 v91, v[24:27]
	s_waitcnt vmcnt(9)
	ds_write_b128 v92, v[28:31]
	s_waitcnt vmcnt(8)
	ds_write_b128 v93, v[32:35]
	s_waitcnt vmcnt(7)
	ds_write_b128 v94, v[36:39]
	s_waitcnt vmcnt(6)
	ds_write_b128 v95, v[80:83]
	s_waitcnt vmcnt(5)
	ds_write_b128 v99, v[122:125]
	s_waitcnt vmcnt(4)
	ds_write_b128 v100, v[126:129]
	s_waitcnt vmcnt(3)
	ds_write_b128 v101, v[130:133]
	s_waitcnt vmcnt(2)
	ds_write_b128 v102, v[134:137]
	s_waitcnt vmcnt(1)
	ds_write_b128 v103, v[138:141]
	s_waitcnt vmcnt(0)
	ds_write_b128 v104, v[142:145]
	v_lshl_add_u32 v80, s13, 7, v48
	v_mov_b64_e32 v[4:5], s[6:7]
	v_mad_i64_i32 v[82:83], s[2:3], v80, s86, v[4:5]
	v_lshl_add_u64 v[4:5], v[82:83], 0, s[46:47]
	v_lshl_add_u64 v[4:5], v[4:5], 0, v[52:53]
	s_mov_b64 s[2:3], 0x3de01400
	v_lshl_add_u64 v[6:7], v[4:5], 0, s[2:3]
	s_mov_b32 s2, 0x3de01000
	v_add_co_u32_e32 v4, vcc, s2, v4
	s_waitcnt lgkmcnt(0)
	s_nop 0
	v_addc_co_u32_e32 v5, vcc, 0, v5, vcc
	s_barrier
	global_load_dwordx4 v[12:15], v[4:5], off offset:1024
	global_load_dwordx4 v[16:19], v[6:7], off offset:64
	global_load_dwordx4 v[8:11], v[6:7], off offset:128
	s_nop 0
	global_load_dwordx4 v[4:7], v[6:7], off offset:192
	ds_read_b128 v[20:23], v51
	ds_read_b128 v[24:27], v51 offset:4096
	ds_read_b128 v[28:31], v51 offset:8192
	ds_read_b128 v[32:35], v51 offset:12288
	ds_read_b128 v[36:39], v51 offset:16384
	ds_read_b128 v[122:125], v51 offset:20480
	ds_read_b128 v[126:129], v51 offset:24576
	ds_read_b128 v[130:133], v51 offset:28672
	ds_read_b128 v[134:137], v51 offset:32768
	ds_read_b128 v[138:141], v51 offset:36864
	ds_read_b128 v[142:145], v51 offset:40960
	ds_read_b128 v[146:149], v51 offset:45056
	ds_read_b128 v[150:153], v51 offset:49152
	ds_read_b128 v[154:157], v51 offset:53248
	ds_read_b128 v[158:161], v51 offset:57344
	ds_read_b128 v[162:165], v51 offset:61440
	v_add_u32_e32 v51, v1, v96
	s_mov_b32 s2, 0xff61b1e6
	v_ashrrev_i32_e32 v81, 31, v80
	s_waitcnt vmcnt(3) lgkmcnt(14)
	v_mfma_f32_16x16x32_bf16 v[20:23], v[20:23], v[12:15], 0
	v_mfma_f32_16x16x32_bf16 v[24:27], v[24:27], v[12:15], 0
	s_waitcnt lgkmcnt(13)
	v_mfma_f32_16x16x32_bf16 v[28:31], v[28:31], v[12:15], 0
	s_waitcnt lgkmcnt(12)
	v_mfma_f32_16x16x32_bf16 v[32:35], v[32:35], v[12:15], 0
	s_waitcnt lgkmcnt(11)
	v_mfma_f32_16x16x32_bf16 v[36:39], v[36:39], v[12:15], 0
	s_waitcnt lgkmcnt(10)
	v_mfma_f32_16x16x32_bf16 v[122:125], v[122:125], v[12:15], 0
	s_waitcnt lgkmcnt(9)
	v_mfma_f32_16x16x32_bf16 v[126:129], v[126:129], v[12:15], 0
	s_waitcnt lgkmcnt(8)
	v_mfma_f32_16x16x32_bf16 v[130:133], v[130:133], v[12:15], 0
	s_waitcnt lgkmcnt(7)
	v_mfma_f32_16x16x32_bf16 v[134:137], v[134:137], v[12:15], 0
	s_waitcnt lgkmcnt(6)
	v_mfma_f32_16x16x32_bf16 v[138:141], v[138:141], v[12:15], 0
	s_waitcnt lgkmcnt(5)
	v_mfma_f32_16x16x32_bf16 v[142:145], v[142:145], v[12:15], 0
	s_waitcnt lgkmcnt(4)
	v_mfma_f32_16x16x32_bf16 v[146:149], v[146:149], v[12:15], 0
	s_waitcnt lgkmcnt(3)
	v_mfma_f32_16x16x32_bf16 v[150:153], v[150:153], v[12:15], 0
	s_waitcnt lgkmcnt(2)
	v_mfma_f32_16x16x32_bf16 v[154:157], v[154:157], v[12:15], 0
	s_waitcnt lgkmcnt(1)
	v_mfma_f32_16x16x32_bf16 v[158:161], v[158:161], v[12:15], 0
	s_waitcnt lgkmcnt(0)
	v_mfma_f32_16x16x32_bf16 v[12:15], v[162:165], v[12:15], 0
	ds_read_b128 v[188:191], v51
	ds_read_b128 v[192:195], v51 offset:4096
	ds_read_b128 v[204:207], v51 offset:8192
	ds_read_b128 v[208:211], v51 offset:12288
	ds_read_b128 v[212:215], v51 offset:16384
	ds_read_b128 v[226:229], v51 offset:20480
	ds_read_b128 v[230:233], v51 offset:24576
	ds_read_b128 v[234:237], v51 offset:28672
	s_waitcnt vmcnt(2) lgkmcnt(7)
	v_mfma_f32_16x16x32_bf16 v[20:23], v[188:191], v[16:19], v[20:23]
	s_waitcnt lgkmcnt(6)
	v_mfma_f32_16x16x32_bf16 v[24:27], v[192:195], v[16:19], v[24:27]
	s_waitcnt lgkmcnt(5)
	v_mfma_f32_16x16x32_bf16 v[28:31], v[204:207], v[16:19], v[28:31]
	s_waitcnt lgkmcnt(4)
	v_mfma_f32_16x16x32_bf16 v[32:35], v[208:211], v[16:19], v[32:35]
	s_waitcnt lgkmcnt(3)
	v_mfma_f32_16x16x32_bf16 v[36:39], v[212:215], v[16:19], v[36:39]
	s_waitcnt lgkmcnt(2)
	v_mfma_f32_16x16x32_bf16 v[122:125], v[226:229], v[16:19], v[122:125]
	s_waitcnt lgkmcnt(1)
	v_mfma_f32_16x16x32_bf16 v[126:129], v[230:233], v[16:19], v[126:129]
	s_waitcnt lgkmcnt(0)
	v_mfma_f32_16x16x32_bf16 v[130:133], v[234:237], v[16:19], v[130:133]
	ds_read_b128 v[188:191], v51 offset:32768
	ds_read_b128 v[192:195], v51 offset:36864
	ds_read_b128 v[204:207], v51 offset:40960
	ds_read_b128 v[208:211], v51 offset:45056
	ds_read_b128 v[212:215], v51 offset:49152
	ds_read_b128 v[226:229], v51 offset:53248
	ds_read_b128 v[230:233], v51 offset:57344
	s_waitcnt lgkmcnt(6)
	v_mfma_f32_16x16x32_bf16 v[134:137], v[188:191], v[16:19], v[134:137]
	s_waitcnt lgkmcnt(5)
	v_mfma_f32_16x16x32_bf16 v[138:141], v[192:195], v[16:19], v[138:141]
	s_waitcnt lgkmcnt(4)
	v_mfma_f32_16x16x32_bf16 v[142:145], v[204:207], v[16:19], v[142:145]
	s_waitcnt lgkmcnt(3)
	v_mfma_f32_16x16x32_bf16 v[146:149], v[208:211], v[16:19], v[146:149]
	s_waitcnt lgkmcnt(2)
	v_mfma_f32_16x16x32_bf16 v[150:153], v[212:215], v[16:19], v[150:153]
	s_waitcnt lgkmcnt(1)
	v_mfma_f32_16x16x32_bf16 v[154:157], v[226:229], v[16:19], v[154:157]
	s_waitcnt lgkmcnt(0)
	v_mfma_f32_16x16x32_bf16 v[158:161], v[230:233], v[16:19], v[158:161]
	ds_read_b128 v[162:165], v51 offset:61440
	v_add_u32_e32 v51, v1, v97
	s_waitcnt lgkmcnt(0)
	v_mfma_f32_16x16x32_bf16 v[12:15], v[162:165], v[16:19], v[12:15]
	ds_read_b128 v[188:191], v51
	ds_read_b128 v[192:195], v51 offset:4096
	ds_read_b128 v[204:207], v51 offset:8192
	ds_read_b128 v[208:211], v51 offset:12288
	ds_read_b128 v[212:215], v51 offset:16384
	ds_read_b128 v[226:229], v51 offset:20480
	ds_read_b128 v[230:233], v51 offset:24576
	ds_read_b128 v[234:237], v51 offset:28672
	s_waitcnt vmcnt(1) lgkmcnt(7)
	v_mfma_f32_16x16x32_bf16 v[16:19], v[188:191], v[8:11], v[20:23]
	s_waitcnt lgkmcnt(6)
	v_mfma_f32_16x16x32_bf16 v[20:23], v[192:195], v[8:11], v[24:27]
	s_waitcnt lgkmcnt(5)
	v_mfma_f32_16x16x32_bf16 v[24:27], v[204:207], v[8:11], v[28:31]
	s_waitcnt lgkmcnt(4)
	v_mfma_f32_16x16x32_bf16 v[28:31], v[208:211], v[8:11], v[32:35]
	s_waitcnt lgkmcnt(3)
	v_mfma_f32_16x16x32_bf16 v[32:35], v[212:215], v[8:11], v[36:39]
	s_waitcnt lgkmcnt(2)
	v_mfma_f32_16x16x32_bf16 v[36:39], v[226:229], v[8:11], v[122:125]
	s_waitcnt lgkmcnt(1)
	v_mfma_f32_16x16x32_bf16 v[122:125], v[230:233], v[8:11], v[126:129]
	s_waitcnt lgkmcnt(0)
	v_mfma_f32_16x16x32_bf16 v[126:129], v[234:237], v[8:11], v[130:133]
	ds_read_b128 v[188:191], v51 offset:32768
	ds_read_b128 v[192:195], v51 offset:36864
	ds_read_b128 v[204:207], v51 offset:40960
	ds_read_b128 v[208:211], v51 offset:45056
	ds_read_b128 v[212:215], v51 offset:49152
	ds_read_b128 v[226:229], v51 offset:53248
	ds_read_b128 v[230:233], v51 offset:57344
	s_waitcnt lgkmcnt(6)
	v_mfma_f32_16x16x32_bf16 v[130:133], v[188:191], v[8:11], v[134:137]
	s_waitcnt lgkmcnt(5)
	v_mfma_f32_16x16x32_bf16 v[134:137], v[192:195], v[8:11], v[138:141]
	s_waitcnt lgkmcnt(4)
	v_mfma_f32_16x16x32_bf16 v[138:141], v[204:207], v[8:11], v[142:145]
	s_waitcnt lgkmcnt(3)
	v_mfma_f32_16x16x32_bf16 v[142:145], v[208:211], v[8:11], v[146:149]
	s_waitcnt lgkmcnt(2)
	v_mfma_f32_16x16x32_bf16 v[146:149], v[212:215], v[8:11], v[150:153]
	s_waitcnt lgkmcnt(1)
	v_mfma_f32_16x16x32_bf16 v[150:153], v[226:229], v[8:11], v[154:157]
	s_waitcnt lgkmcnt(0)
	v_mfma_f32_16x16x32_bf16 v[154:157], v[230:233], v[8:11], v[158:161]
	ds_read_b128 v[158:161], v51 offset:61440
	v_add_u32_e32 v51, v1, v98
	s_waitcnt lgkmcnt(0)
	v_mfma_f32_16x16x32_bf16 v[158:161], v[158:161], v[8:11], v[12:15]
	ds_read_b128 v[8:11], v51
	s_waitcnt vmcnt(0) lgkmcnt(0)
	v_mfma_f32_16x16x32_bf16 v[162:165], v[8:11], v[4:7], v[16:19]
	ds_read_b128 v[8:11], v51 offset:4096
	s_nop 6
	v_max_f32_e32 v53, v164, v164
	s_waitcnt lgkmcnt(0)
	v_mfma_f32_16x16x32_bf16 v[166:169], v[8:11], v[4:7], v[20:23]
	ds_read_b128 v[8:11], v51 offset:8192
	s_nop 6
	v_max_f32_e32 v55, v168, v168
	s_waitcnt lgkmcnt(0)
	v_mfma_f32_16x16x32_bf16 v[170:173], v[8:11], v[4:7], v[24:27]
	ds_read_b128 v[8:11], v51 offset:12288
	s_waitcnt lgkmcnt(0)
	v_mfma_f32_16x16x32_bf16 v[174:177], v[8:11], v[4:7], v[28:31]
	ds_read_b128 v[8:11], v51 offset:16384
	s_nop 6
	v_max_f32_e32 v121, v176, v176
	s_waitcnt lgkmcnt(0)
	v_mfma_f32_16x16x32_bf16 v[178:181], v[8:11], v[4:7], v[32:35]
	ds_read_b128 v[188:191], v51 offset:20480
	ds_read_b128 v[192:195], v51 offset:24576
	ds_read_b128 v[204:207], v51 offset:28672
	s_waitcnt lgkmcnt(2)
	v_mfma_f32_16x16x32_bf16 v[182:185], v[188:191], v[4:7], v[36:39]
	s_waitcnt lgkmcnt(1)
	v_mfma_f32_16x16x32_bf16 v[122:125], v[192:195], v[4:7], v[122:125]
	s_waitcnt lgkmcnt(0)
	v_mfma_f32_16x16x32_bf16 v[36:39], v[204:207], v[4:7], v[126:129]
	ds_read_b128 v[8:11], v51 offset:32768
	s_nop 1
	ds_read_b128 v[126:129], v51 offset:61440
	s_waitcnt lgkmcnt(1)
	v_mfma_f32_16x16x32_bf16 v[32:35], v[8:11], v[4:7], v[130:133]
	ds_read_b128 v[188:191], v51 offset:36864
	ds_read_b128 v[192:195], v51 offset:40960
	ds_read_b128 v[204:207], v51 offset:45056
	ds_read_b128 v[208:211], v51 offset:49152
	ds_read_b128 v[212:215], v51 offset:53248
	s_waitcnt lgkmcnt(4)
	v_mfma_f32_16x16x32_bf16 v[28:31], v[188:191], v[4:7], v[134:137]
	s_waitcnt lgkmcnt(3)
	v_mfma_f32_16x16x32_bf16 v[24:27], v[192:195], v[4:7], v[138:141]
	s_waitcnt lgkmcnt(2)
	v_mfma_f32_16x16x32_bf16 v[20:23], v[204:207], v[4:7], v[142:145]
	s_waitcnt lgkmcnt(1)
	v_mfma_f32_16x16x32_bf16 v[16:19], v[208:211], v[4:7], v[146:149]
	s_waitcnt lgkmcnt(0)
	v_mfma_f32_16x16x32_bf16 v[12:15], v[212:215], v[4:7], v[150:153]
	ds_read_b128 v[8:11], v51 offset:57344
	v_max_f32_e32 v51, v165, v165
	v_max_f32_e32 v51, v53, v51
	v_max_f32_e32 v53, v169, v169
	v_max_f32_e32 v53, v55, v53
	v_max3_f32 v51, v162, v163, v51
	v_max3_f32 v53, v166, v167, v53
	v_max3_f32 v51, v51, s2, v53
	v_max_f32_e32 v53, v173, v173
	v_max_f32_e32 v55, v172, v172
	v_max_f32_e32 v53, v55, v53
	v_max_f32_e32 v55, v177, v177
	v_max_f32_e32 v55, v121, v55
	v_max3_f32 v53, v170, v171, v53
	v_max3_f32 v55, v174, v175, v55
	v_max3_f32 v51, v51, v53, v55
	v_max_f32_e32 v53, v181, v181
	v_max_f32_e32 v55, v180, v180
	v_max_f32_e32 v53, v55, v53
	v_max_f32_e32 v55, v185, v185
	v_max_f32_e32 v121, v184, v184
	v_max_f32_e32 v55, v121, v55
	v_max3_f32 v53, v178, v179, v53
	v_max3_f32 v55, v182, v183, v55
	v_max3_f32 v51, v51, v53, v55
	v_max_f32_e32 v53, v125, v125
	v_max_f32_e32 v55, v124, v124
	v_max_f32_e32 v53, v55, v53
	v_max_f32_e32 v55, v39, v39
	v_max_f32_e32 v121, v38, v38
	v_max_f32_e32 v55, v121, v55
	v_max3_f32 v53, v122, v123, v53
	v_max3_f32 v55, v36, v37, v55
	v_max3_f32 v51, v51, v53, v55
	v_max_f32_e32 v53, v35, v35
	v_max_f32_e32 v55, v34, v34
	v_max_f32_e32 v53, v55, v53
	v_max_f32_e32 v55, v31, v31
	v_max_f32_e32 v121, v30, v30
	v_max_f32_e32 v55, v121, v55
	v_max3_f32 v53, v32, v33, v53
	v_max3_f32 v55, v28, v29, v55
	v_max3_f32 v51, v51, v53, v55
	v_max_f32_e32 v53, v27, v27
	v_max_f32_e32 v55, v26, v26
	v_max_f32_e32 v53, v55, v53
	v_max_f32_e32 v55, v23, v23
	v_max_f32_e32 v121, v22, v22
	v_max_f32_e32 v55, v121, v55
	v_max3_f32 v53, v24, v25, v53
	v_max3_f32 v55, v20, v21, v55
	s_waitcnt lgkmcnt(0)
	v_mfma_f32_16x16x32_bf16 v[8:11], v[8:11], v[4:7], v[154:157]
	v_max3_f32 v51, v51, v53, v55
	v_max_f32_e32 v53, v19, v19
	v_max_f32_e32 v55, v18, v18
	v_mfma_f32_16x16x32_bf16 v[4:7], v[126:129], v[4:7], v[158:161]
	v_max_f32_e32 v53, v55, v53
	v_max_f32_e32 v55, v15, v15
	v_max_f32_e32 v121, v14, v14
	v_max_f32_e32 v55, v121, v55
	v_max3_f32 v53, v16, v17, v53
	v_max3_f32 v55, v12, v13, v55
	v_max3_f32 v51, v51, v53, v55
	v_max_f32_e32 v53, v11, v11
	v_max_f32_e32 v55, v10, v10
	v_max_f32_e32 v53, v55, v53
	v_max_f32_e32 v55, v7, v7
	v_max_f32_e32 v121, v6, v6
	v_max_f32_e32 v55, v121, v55
	v_max3_f32 v53, v8, v9, v53
	v_max3_f32 v55, v4, v5, v55
	v_max3_f32 v51, v51, v53, v55
	ds_bpermute_b32 v53, v84, v51
	s_waitcnt lgkmcnt(0)
	v_max_f32_e32 v53, v53, v53
	v_max_f32_e32 v51, v51, v53
	ds_bpermute_b32 v53, v85, v51
	s_waitcnt lgkmcnt(0)
	v_max_f32_e32 v53, v53, v53
	v_max_f32_e32 v51, v51, v53
	v_sub_f32_e32 v53, v162, v51
	v_mul_f32_e32 v53, 0x3e0293ee, v53
	v_sub_f32_e32 v121, v163, v51
	v_exp_f32_e32 v53, v53
	v_mul_f32_e32 v121, 0x3e0293ee, v121
	v_sub_f32_e32 v126, v164, v51
	v_exp_f32_e32 v121, v121
	v_mul_f32_e32 v126, 0x3e0293ee, v126
	v_sub_f32_e32 v127, v165, v51
	v_exp_f32_e32 v126, v126
	v_mul_f32_e32 v127, 0x3e0293ee, v127
	v_sub_f32_e32 v128, v166, v51
	v_exp_f32_e32 v127, v127
	v_mul_f32_e32 v128, 0x3e0293ee, v128
	v_sub_f32_e32 v129, v167, v51
	v_add_f32_e32 v55, 0, v53
	v_exp_f32_e32 v128, v128
	v_mul_f32_e32 v129, 0x3e0293ee, v129
	v_sub_f32_e32 v130, v168, v51
	v_add_f32_e32 v55, v121, v55
	v_exp_f32_e32 v129, v129
	v_mul_f32_e32 v130, 0x3e0293ee, v130
	v_sub_f32_e32 v131, v169, v51
	v_add_f32_e32 v55, v126, v55
	v_exp_f32_e32 v130, v130
	v_mul_f32_e32 v131, 0x3e0293ee, v131
	v_sub_f32_e32 v132, v170, v51
	v_add_f32_e32 v55, v127, v55
	v_exp_f32_e32 v131, v131
	v_mul_f32_e32 v132, 0x3e0293ee, v132
	v_sub_f32_e32 v133, v171, v51
	v_add_f32_e32 v55, v128, v55
	v_exp_f32_e32 v132, v132
	v_mul_f32_e32 v133, 0x3e0293ee, v133
	v_sub_f32_e32 v134, v172, v51
	v_add_f32_e32 v55, v129, v55
	v_exp_f32_e32 v133, v133
	v_mul_f32_e32 v134, 0x3e0293ee, v134
	v_sub_f32_e32 v135, v173, v51
	v_add_f32_e32 v55, v130, v55
	v_exp_f32_e32 v134, v134
	v_mul_f32_e32 v135, 0x3e0293ee, v135
	v_sub_f32_e32 v136, v174, v51
	v_add_f32_e32 v55, v131, v55
	v_exp_f32_e32 v135, v135
	v_mul_f32_e32 v136, 0x3e0293ee, v136
	v_sub_f32_e32 v137, v175, v51
	v_add_f32_e32 v55, v132, v55
	v_exp_f32_e32 v136, v136
	v_mul_f32_e32 v137, 0x3e0293ee, v137
	v_sub_f32_e32 v138, v176, v51
	v_add_f32_e32 v55, v133, v55
	v_exp_f32_e32 v137, v137
	v_mul_f32_e32 v138, 0x3e0293ee, v138
	v_sub_f32_e32 v139, v177, v51
	v_add_f32_e32 v55, v134, v55
	v_exp_f32_e32 v138, v138
	v_mul_f32_e32 v139, 0x3e0293ee, v139
	v_sub_f32_e32 v140, v178, v51
	v_add_f32_e32 v55, v135, v55
	v_exp_f32_e32 v139, v139
	v_mul_f32_e32 v140, 0x3e0293ee, v140
	v_sub_f32_e32 v141, v179, v51
	v_add_f32_e32 v55, v136, v55
	v_exp_f32_e32 v140, v140
	v_mul_f32_e32 v141, 0x3e0293ee, v141
	v_sub_f32_e32 v142, v180, v51
	v_add_f32_e32 v55, v137, v55
	v_exp_f32_e32 v141, v141
	v_mul_f32_e32 v142, 0x3e0293ee, v142
	v_sub_f32_e32 v143, v181, v51
	v_add_f32_e32 v55, v138, v55
	v_exp_f32_e32 v142, v142
	v_mul_f32_e32 v143, 0x3e0293ee, v143
	v_sub_f32_e32 v144, v182, v51
	v_add_f32_e32 v55, v139, v55
	v_exp_f32_e32 v143, v143
	v_mul_f32_e32 v144, 0x3e0293ee, v144
	v_sub_f32_e32 v145, v183, v51
	v_sub_f32_e32 v122, v122, v51
	v_add_f32_e32 v55, v140, v55
	v_exp_f32_e32 v144, v144
	v_mul_f32_e32 v145, 0x3e0293ee, v145
	v_sub_f32_e32 v146, v184, v51
	v_mul_f32_e32 v122, 0x3e0293ee, v122
	v_add_f32_e32 v55, v141, v55
	v_exp_f32_e32 v145, v145
	v_mul_f32_e32 v146, 0x3e0293ee, v146
	v_sub_f32_e32 v147, v185, v51
	v_exp_f32_e32 v148, v122
	v_sub_f32_e32 v122, v123, v51
	v_add_f32_e32 v55, v142, v55
	v_exp_f32_e32 v146, v146
	v_mul_f32_e32 v147, 0x3e0293ee, v147
	v_mul_f32_e32 v122, 0x3e0293ee, v122
	v_add_f32_e32 v55, v143, v55
	v_exp_f32_e32 v147, v147
	v_exp_f32_e32 v149, v122
	v_sub_f32_e32 v122, v124, v51
	v_add_f32_e32 v55, v144, v55
	v_mul_f32_e32 v122, 0x3e0293ee, v122
	v_add_f32_e32 v55, v145, v55
	v_exp_f32_e32 v150, v122
	v_sub_f32_e32 v122, v125, v51
	v_add_f32_e32 v55, v146, v55
	v_mul_f32_e32 v122, 0x3e0293ee, v122
	v_sub_f32_e32 v36, v36, v51
	v_add_f32_e32 v55, v147, v55
	v_exp_f32_e32 v151, v122
	v_mul_f32_e32 v36, 0x3e0293ee, v36
	v_add_f32_e32 v55, v148, v55
	v_exp_f32_e32 v152, v36
	v_add_f32_e32 v55, v149, v55
	v_add_f32_e32 v55, v150, v55
	v_sub_f32_e32 v37, v37, v51
	v_add_f32_e32 v55, v151, v55
	v_mul_f32_e32 v37, 0x3e0293ee, v37
	v_add_f32_e32 v36, v152, v55
	v_exp_f32_e32 v55, v37
	v_sub_f32_e32 v37, v38, v51
	v_mul_f32_e32 v37, 0x3e0293ee, v37
	v_exp_f32_e32 v153, v37
	v_sub_f32_e32 v37, v39, v51
	v_sub_f32_e32 v33, v33, v51
	v_mul_f32_e32 v37, 0x3e0293ee, v37
	v_sub_f32_e32 v32, v32, v51
	v_mul_f32_e32 v33, 0x3e0293ee, v33
	v_exp_f32_e32 v154, v37
	v_mul_f32_e32 v32, 0x3e0293ee, v32
	v_exp_f32_e32 v156, v33
	v_sub_f32_e32 v33, v34, v51
	v_exp_f32_e32 v155, v32
	v_mul_f32_e32 v33, 0x3e0293ee, v33
	v_add_f32_e32 v36, v55, v36
	v_exp_f32_e32 v157, v33
	v_sub_f32_e32 v33, v35, v51
	v_sub_f32_e32 v29, v29, v51
	v_add_f32_e32 v36, v153, v36
	v_mul_f32_e32 v33, 0x3e0293ee, v33
	v_sub_f32_e32 v28, v28, v51
	v_mul_f32_e32 v29, 0x3e0293ee, v29
	v_add_f32_e32 v36, v154, v36
	v_exp_f32_e32 v158, v33
	v_mul_f32_e32 v28, 0x3e0293ee, v28
	v_exp_f32_e32 v160, v29
	v_sub_f32_e32 v29, v30, v51
	v_add_f32_e32 v32, v155, v36
	v_exp_f32_e32 v159, v28
	v_mul_f32_e32 v29, 0x3e0293ee, v29
	v_add_f32_e32 v32, v156, v32
	v_exp_f32_e32 v161, v29
	v_sub_f32_e32 v29, v31, v51
	v_sub_f32_e32 v25, v25, v51
	v_add_f32_e32 v32, v157, v32
	v_mul_f32_e32 v29, 0x3e0293ee, v29
	v_sub_f32_e32 v24, v24, v51
	v_mul_f32_e32 v25, 0x3e0293ee, v25
	v_add_f32_e32 v32, v158, v32
	v_exp_f32_e32 v162, v29
	v_mul_f32_e32 v24, 0x3e0293ee, v24
	v_exp_f32_e32 v164, v25
	v_sub_f32_e32 v25, v26, v51
	v_add_f32_e32 v28, v159, v32
	v_exp_f32_e32 v163, v24
	v_mul_f32_e32 v25, 0x3e0293ee, v25
	v_add_f32_e32 v28, v160, v28
	v_exp_f32_e32 v165, v25
	v_sub_f32_e32 v25, v27, v51
	v_sub_f32_e32 v21, v21, v51
	v_add_f32_e32 v28, v161, v28
	v_mul_f32_e32 v25, 0x3e0293ee, v25
	v_sub_f32_e32 v20, v20, v51
	v_mul_f32_e32 v21, 0x3e0293ee, v21
	v_add_f32_e32 v28, v162, v28
	v_exp_f32_e32 v166, v25
	v_mul_f32_e32 v20, 0x3e0293ee, v20
	v_exp_f32_e32 v168, v21
	v_sub_f32_e32 v21, v22, v51
	v_add_f32_e32 v24, v163, v28
	v_exp_f32_e32 v167, v20
	v_mul_f32_e32 v21, 0x3e0293ee, v21
	v_add_f32_e32 v24, v164, v24
	v_exp_f32_e32 v169, v21
	v_sub_f32_e32 v21, v23, v51
	v_sub_f32_e32 v17, v17, v51
	v_add_f32_e32 v24, v165, v24
	v_mul_f32_e32 v21, 0x3e0293ee, v21
	v_sub_f32_e32 v16, v16, v51
	v_mul_f32_e32 v17, 0x3e0293ee, v17
	v_add_f32_e32 v24, v166, v24
	v_exp_f32_e32 v170, v21
	v_mul_f32_e32 v16, 0x3e0293ee, v16
	v_exp_f32_e32 v172, v17
	v_sub_f32_e32 v17, v18, v51
	v_add_f32_e32 v20, v167, v24
	v_exp_f32_e32 v171, v16
	v_mul_f32_e32 v17, 0x3e0293ee, v17
	v_add_f32_e32 v20, v168, v20
	v_exp_f32_e32 v173, v17
	v_sub_f32_e32 v17, v19, v51
	v_sub_f32_e32 v13, v13, v51
	v_add_f32_e32 v20, v169, v20
	v_mul_f32_e32 v17, 0x3e0293ee, v17
	v_sub_f32_e32 v12, v12, v51
	v_mul_f32_e32 v13, 0x3e0293ee, v13
	v_add_f32_e32 v20, v170, v20
	v_exp_f32_e32 v174, v17
	v_mul_f32_e32 v12, 0x3e0293ee, v12
	v_exp_f32_e32 v176, v13
	v_sub_f32_e32 v13, v14, v51
	v_add_f32_e32 v16, v171, v20
	v_exp_f32_e32 v175, v12
	v_mul_f32_e32 v13, 0x3e0293ee, v13
	v_add_f32_e32 v16, v172, v16
	v_exp_f32_e32 v177, v13
	v_sub_f32_e32 v13, v15, v51
	v_sub_f32_e32 v9, v9, v51
	v_add_f32_e32 v16, v173, v16
	v_mul_f32_e32 v13, 0x3e0293ee, v13
	v_sub_f32_e32 v8, v8, v51
	v_mul_f32_e32 v9, 0x3e0293ee, v9
	v_add_f32_e32 v16, v174, v16
	v_exp_f32_e32 v178, v13
	v_mul_f32_e32 v8, 0x3e0293ee, v8
	v_exp_f32_e32 v180, v9
	v_sub_f32_e32 v9, v10, v51
	v_add_f32_e32 v12, v175, v16
	v_exp_f32_e32 v179, v8
	v_mul_f32_e32 v9, 0x3e0293ee, v9
	v_add_f32_e32 v12, v176, v12
	v_exp_f32_e32 v181, v9
	v_sub_f32_e32 v9, v11, v51
	v_sub_f32_e32 v5, v5, v51
	v_add_f32_e32 v12, v177, v12
	v_mul_f32_e32 v9, 0x3e0293ee, v9
	v_sub_f32_e32 v4, v4, v51
	v_mul_f32_e32 v5, 0x3e0293ee, v5
	v_add_f32_e32 v12, v178, v12
	v_exp_f32_e32 v182, v9
	v_mul_f32_e32 v4, 0x3e0293ee, v4
	v_exp_f32_e32 v184, v5
	v_sub_f32_e32 v5, v6, v51
	v_add_f32_e32 v8, v179, v12
	v_exp_f32_e32 v183, v4
	v_mul_f32_e32 v5, 0x3e0293ee, v5
	v_add_f32_e32 v8, v180, v8
	v_exp_f32_e32 v185, v5
	v_sub_f32_e32 v5, v7, v51
	v_add_f32_e32 v8, v181, v8
	v_mul_f32_e32 v5, 0x3e0293ee, v5
	v_add_f32_e32 v8, v182, v8
	v_exp_f32_e32 v51, v5
	v_add_f32_e32 v4, v183, v8
	v_add_f32_e32 v4, v184, v4
	v_add_f32_e32 v4, v185, v4
	v_add_f32_e32 v4, v51, v4
	ds_bpermute_b32 v5, v84, v4
	s_waitcnt lgkmcnt(0)
	v_add_f32_e32 v4, v4, v5
	ds_bpermute_b32 v5, v85, v4
	s_waitcnt lgkmcnt(0)
	v_add_f32_e32 v186, v4, v5
	v_cvt_pk_bf16_f32 v4, v53, v121
	v_cvt_pk_bf16_f32 v5, v126, v127
	v_cvt_pk_bf16_f32 v6, v128, v129
	v_cvt_pk_bf16_f32 v7, v130, v131
	ds_read2st64_b64 v[8:11], v105 offset1:16
	ds_read2st64_b64 v[12:15], v106 offset1:16
	s_waitcnt lgkmcnt(1)
	v_mov_b32_e32 v16, v8
	s_waitcnt lgkmcnt(0)
	v_mov_b32_e32 v18, v12
	v_mov_b32_e32 v19, v13
	v_mov_b32_e32 v12, v10
	v_mov_b32_e32 v13, v11
	v_mov_b32_e32 v17, v9
	s_nop 0
	v_mfma_f32_16x16x32_bf16 v[8:11], v[12:15], v[4:7], 0
	ds_read2st64_b64 v[12:15], v105 offset0:32 offset1:48
	ds_read2st64_b64 v[20:23], v106 offset0:32 offset1:48
	s_waitcnt lgkmcnt(1)
	v_mov_b32_e32 v24, v12
	s_waitcnt lgkmcnt(0)
	v_mov_b32_e32 v26, v20
	v_mov_b32_e32 v27, v21
	v_mov_b32_e32 v20, v14
	v_mov_b32_e32 v21, v15
	v_mov_b32_e32 v25, v13
	v_mfma_f32_16x16x32_bf16 v[16:19], v[16:19], v[4:7], 0
	v_mfma_f32_16x16x32_bf16 v[12:15], v[20:23], v[4:7], 0
	ds_read2st64_b64 v[20:23], v105 offset0:64 offset1:80
	ds_read2st64_b64 v[28:31], v106 offset0:64 offset1:80
	s_waitcnt lgkmcnt(1)
	v_mov_b32_e32 v32, v20
	s_waitcnt lgkmcnt(0)
	v_mov_b32_e32 v34, v28
	v_mov_b32_e32 v35, v29
	v_mov_b32_e32 v28, v22
	v_mov_b32_e32 v29, v23
	v_mov_b32_e32 v33, v21
	v_mfma_f32_16x16x32_bf16 v[24:27], v[24:27], v[4:7], 0
	v_mfma_f32_16x16x32_bf16 v[20:23], v[28:31], v[4:7], 0
	ds_read2st64_b64 v[28:31], v105 offset0:96 offset1:112
	ds_read2st64_b64 v[36:39], v106 offset0:96 offset1:112
	s_waitcnt lgkmcnt(1)
	v_mov_b32_e32 v122, v28
	v_mov_b32_e32 v123, v29
	s_waitcnt lgkmcnt(0)
	v_mov_b32_e32 v124, v36
	v_mov_b32_e32 v125, v37
	v_mov_b32_e32 v36, v30
	v_mov_b32_e32 v37, v31
	v_mfma_f32_16x16x32_bf16 v[32:35], v[32:35], v[4:7], 0
	v_cvt_pk_bf16_f32 v28, v132, v133
	v_cvt_pk_bf16_f32 v29, v134, v135
	v_cvt_pk_bf16_f32 v30, v136, v137
	v_mfma_f32_16x16x32_bf16 v[122:125], v[122:125], v[4:7], 0
	v_cvt_pk_bf16_f32 v31, v138, v139
	v_mfma_f32_16x16x32_bf16 v[4:7], v[36:39], v[4:7], 0
	ds_read2st64_b64 v[36:39], v107 offset1:16
	ds_read2st64_b64 v[126:129], v108 offset1:16
	s_waitcnt lgkmcnt(1)
	v_mov_b32_e32 v130, v36
	s_waitcnt lgkmcnt(0)
	v_mov_b32_e32 v132, v126
	v_mov_b32_e32 v133, v127
	v_mov_b32_e32 v126, v38
	v_mov_b32_e32 v127, v39
	v_mov_b32_e32 v131, v37
	s_nop 0
	v_mfma_f32_16x16x32_bf16 v[8:11], v[126:129], v[28:31], v[8:11]
	ds_read2st64_b64 v[36:39], v107 offset0:32 offset1:48
	ds_read2st64_b64 v[126:129], v108 offset0:32 offset1:48
	v_mfma_f32_16x16x32_bf16 v[16:19], v[130:133], v[28:31], v[16:19]
	s_waitcnt lgkmcnt(1)
	v_mov_b32_e32 v130, v36
	s_waitcnt lgkmcnt(0)
	v_mov_b32_e32 v132, v126
	v_mov_b32_e32 v133, v127
	v_mov_b32_e32 v126, v38
	v_mov_b32_e32 v127, v39
	v_mov_b32_e32 v131, v37
	s_nop 0
	v_mfma_f32_16x16x32_bf16 v[12:15], v[126:129], v[28:31], v[12:15]
	ds_read2st64_b64 v[36:39], v107 offset0:64 offset1:80
	ds_read2st64_b64 v[126:129], v108 offset0:64 offset1:80
	v_mfma_f32_16x16x32_bf16 v[24:27], v[130:133], v[28:31], v[24:27]
	s_waitcnt lgkmcnt(1)
	v_mov_b32_e32 v130, v36
	s_waitcnt lgkmcnt(0)
	v_mov_b32_e32 v132, v126
	v_mov_b32_e32 v133, v127
	v_mov_b32_e32 v126, v38
	v_mov_b32_e32 v127, v39
	v_mov_b32_e32 v131, v37
	s_nop 0
	v_mfma_f32_16x16x32_bf16 v[20:23], v[126:129], v[28:31], v[20:23]
	ds_read2st64_b64 v[36:39], v107 offset0:96 offset1:112
	ds_read2st64_b64 v[126:129], v108 offset0:96 offset1:112
	v_mfma_f32_16x16x32_bf16 v[32:35], v[130:133], v[28:31], v[32:35]
	s_waitcnt lgkmcnt(1)
	v_mov_b32_e32 v130, v36
	v_mov_b32_e32 v131, v37
	s_waitcnt lgkmcnt(0)
	v_mov_b32_e32 v132, v126
	v_mov_b32_e32 v133, v127
	v_mov_b32_e32 v126, v38
	v_mov_b32_e32 v127, v39
	v_mfma_f32_16x16x32_bf16 v[122:125], v[130:133], v[28:31], v[122:125]
	s_nop 0
	v_mfma_f32_16x16x32_bf16 v[4:7], v[126:129], v[28:31], v[4:7]
	v_cvt_pk_bf16_f32 v28, v140, v141
	v_cvt_pk_bf16_f32 v29, v142, v143
	v_cvt_pk_bf16_f32 v30, v144, v145
	v_cvt_pk_bf16_f32 v31, v146, v147
	ds_read2st64_b64 v[36:39], v109 offset1:16
	ds_read2st64_b64 v[126:129], v110 offset1:16
	s_waitcnt lgkmcnt(1)
	v_mov_b32_e32 v130, v36
	s_waitcnt lgkmcnt(0)
	v_mov_b32_e32 v132, v126
	v_mov_b32_e32 v133, v127
	v_mov_b32_e32 v126, v38
	v_mov_b32_e32 v127, v39
	v_mov_b32_e32 v131, v37
	s_nop 0
	v_mfma_f32_16x16x32_bf16 v[8:11], v[126:129], v[28:31], v[8:11]
	ds_read2st64_b64 v[36:39], v109 offset0:32 offset1:48
	ds_read2st64_b64 v[126:129], v110 offset0:32 offset1:48
	v_mfma_f32_16x16x32_bf16 v[16:19], v[130:133], v[28:31], v[16:19]
	s_waitcnt lgkmcnt(1)
	v_mov_b32_e32 v130, v36
	s_waitcnt lgkmcnt(0)
	v_mov_b32_e32 v132, v126
	v_mov_b32_e32 v133, v127
	v_mov_b32_e32 v126, v38
	v_mov_b32_e32 v127, v39
	v_mov_b32_e32 v131, v37
	s_nop 0
	v_mfma_f32_16x16x32_bf16 v[12:15], v[126:129], v[28:31], v[12:15]
	ds_read2st64_b64 v[36:39], v109 offset0:64 offset1:80
	ds_read2st64_b64 v[126:129], v110 offset0:64 offset1:80
	v_mfma_f32_16x16x32_bf16 v[24:27], v[130:133], v[28:31], v[24:27]
	s_waitcnt lgkmcnt(1)
	v_mov_b32_e32 v130, v36
	s_waitcnt lgkmcnt(0)
	v_mov_b32_e32 v132, v126
	v_mov_b32_e32 v133, v127
	v_mov_b32_e32 v126, v38
	v_mov_b32_e32 v127, v39
	v_mov_b32_e32 v131, v37
	s_nop 0
	v_mfma_f32_16x16x32_bf16 v[20:23], v[126:129], v[28:31], v[20:23]
	ds_read2st64_b64 v[36:39], v109 offset0:96 offset1:112
	ds_read2st64_b64 v[126:129], v110 offset0:96 offset1:112
	v_mfma_f32_16x16x32_bf16 v[32:35], v[130:133], v[28:31], v[32:35]
	s_waitcnt lgkmcnt(1)
	v_mov_b32_e32 v130, v36
	v_mov_b32_e32 v131, v37
	s_waitcnt lgkmcnt(0)
	v_mov_b32_e32 v132, v126
	v_mov_b32_e32 v133, v127
	v_mov_b32_e32 v126, v38
	v_mov_b32_e32 v127, v39
	v_mfma_f32_16x16x32_bf16 v[122:125], v[130:133], v[28:31], v[122:125]
	s_nop 0
	v_mfma_f32_16x16x32_bf16 v[4:7], v[126:129], v[28:31], v[4:7]
	v_cvt_pk_bf16_f32 v28, v148, v149
	v_cvt_pk_bf16_f32 v29, v150, v151
	v_cvt_pk_bf16_f32 v30, v152, v55
	v_cvt_pk_bf16_f32 v31, v153, v154
	ds_read2st64_b64 v[36:39], v111 offset1:16
	ds_read2st64_b64 v[126:129], v112 offset1:16
	s_waitcnt lgkmcnt(1)
	v_mov_b32_e32 v130, v36
	s_waitcnt lgkmcnt(0)
	v_mov_b32_e32 v132, v126
	v_mov_b32_e32 v133, v127
	v_mov_b32_e32 v126, v38
	v_mov_b32_e32 v127, v39
	v_mov_b32_e32 v131, v37
	s_nop 0
	v_mfma_f32_16x16x32_bf16 v[8:11], v[126:129], v[28:31], v[8:11]
	ds_read2st64_b64 v[36:39], v111 offset0:32 offset1:48
	ds_read2st64_b64 v[126:129], v112 offset0:32 offset1:48
	v_mfma_f32_16x16x32_bf16 v[16:19], v[130:133], v[28:31], v[16:19]
	s_waitcnt lgkmcnt(1)
	v_mov_b32_e32 v130, v36
	s_waitcnt lgkmcnt(0)
	v_mov_b32_e32 v132, v126
	v_mov_b32_e32 v133, v127
	v_mov_b32_e32 v126, v38
	v_mov_b32_e32 v127, v39
	v_mov_b32_e32 v131, v37
	s_nop 0
	v_mfma_f32_16x16x32_bf16 v[12:15], v[126:129], v[28:31], v[12:15]
	ds_read2st64_b64 v[36:39], v111 offset0:64 offset1:80
	ds_read2st64_b64 v[126:129], v112 offset0:64 offset1:80
	v_mfma_f32_16x16x32_bf16 v[24:27], v[130:133], v[28:31], v[24:27]
	s_waitcnt lgkmcnt(1)
	v_mov_b32_e32 v130, v36
	s_waitcnt lgkmcnt(0)
	v_mov_b32_e32 v132, v126
	v_mov_b32_e32 v133, v127
	v_mov_b32_e32 v126, v38
	v_mov_b32_e32 v127, v39
	v_mov_b32_e32 v131, v37
	s_nop 0
	v_mfma_f32_16x16x32_bf16 v[20:23], v[126:129], v[28:31], v[20:23]
	ds_read2st64_b64 v[36:39], v111 offset0:96 offset1:112
	ds_read2st64_b64 v[126:129], v112 offset0:96 offset1:112
	v_mfma_f32_16x16x32_bf16 v[32:35], v[130:133], v[28:31], v[32:35]
	s_waitcnt lgkmcnt(1)
	v_mov_b32_e32 v130, v36
	v_mov_b32_e32 v131, v37
	s_waitcnt lgkmcnt(0)
	v_mov_b32_e32 v132, v126
	v_mov_b32_e32 v133, v127
	v_mov_b32_e32 v126, v38
	v_mov_b32_e32 v127, v39
	v_mfma_f32_16x16x32_bf16 v[122:125], v[130:133], v[28:31], v[122:125]
	s_nop 0
	v_mfma_f32_16x16x32_bf16 v[4:7], v[126:129], v[28:31], v[4:7]
	v_cvt_pk_bf16_f32 v28, v155, v156
	v_cvt_pk_bf16_f32 v29, v157, v158
	v_cvt_pk_bf16_f32 v30, v159, v160
	v_cvt_pk_bf16_f32 v31, v161, v162
	ds_read2st64_b64 v[36:39], v113 offset1:16
	ds_read2st64_b64 v[126:129], v114 offset1:16
	s_waitcnt lgkmcnt(1)
	v_mov_b32_e32 v130, v36
	s_waitcnt lgkmcnt(0)
	v_mov_b32_e32 v132, v126
	v_mov_b32_e32 v133, v127
	v_mov_b32_e32 v126, v38
	v_mov_b32_e32 v127, v39
	v_mov_b32_e32 v131, v37
	s_nop 0
	v_mfma_f32_16x16x32_bf16 v[8:11], v[126:129], v[28:31], v[8:11]
	ds_read2st64_b64 v[36:39], v113 offset0:32 offset1:48
	ds_read2st64_b64 v[126:129], v114 offset0:32 offset1:48
	v_mfma_f32_16x16x32_bf16 v[16:19], v[130:133], v[28:31], v[16:19]
	s_waitcnt lgkmcnt(1)
	v_mov_b32_e32 v130, v36
	s_waitcnt lgkmcnt(0)
	v_mov_b32_e32 v132, v126
	v_mov_b32_e32 v133, v127
	v_mov_b32_e32 v126, v38
	v_mov_b32_e32 v127, v39
	v_mov_b32_e32 v131, v37
	s_nop 0
	v_mfma_f32_16x16x32_bf16 v[12:15], v[126:129], v[28:31], v[12:15]
	ds_read2st64_b64 v[36:39], v113 offset0:64 offset1:80
	ds_read2st64_b64 v[126:129], v114 offset0:64 offset1:80
	v_mfma_f32_16x16x32_bf16 v[24:27], v[130:133], v[28:31], v[24:27]
	s_waitcnt lgkmcnt(1)
	v_mov_b32_e32 v130, v36
	s_waitcnt lgkmcnt(0)
	v_mov_b32_e32 v132, v126
	v_mov_b32_e32 v133, v127
	v_mov_b32_e32 v126, v38
	v_mov_b32_e32 v127, v39
	v_mov_b32_e32 v131, v37
	s_nop 0
	v_mfma_f32_16x16x32_bf16 v[20:23], v[126:129], v[28:31], v[20:23]
	ds_read2st64_b64 v[36:39], v113 offset0:96 offset1:112
	ds_read2st64_b64 v[126:129], v114 offset0:96 offset1:112
	v_mfma_f32_16x16x32_bf16 v[32:35], v[130:133], v[28:31], v[32:35]
	s_waitcnt lgkmcnt(1)
	v_mov_b32_e32 v130, v36
	v_mov_b32_e32 v131, v37
	s_waitcnt lgkmcnt(0)
	v_mov_b32_e32 v132, v126
	v_mov_b32_e32 v133, v127
	v_mov_b32_e32 v126, v38
	v_mov_b32_e32 v127, v39
	v_mfma_f32_16x16x32_bf16 v[122:125], v[130:133], v[28:31], v[122:125]
	s_nop 0
	v_mfma_f32_16x16x32_bf16 v[4:7], v[126:129], v[28:31], v[4:7]
	v_cvt_pk_bf16_f32 v28, v163, v164
	v_cvt_pk_bf16_f32 v29, v165, v166
	v_cvt_pk_bf16_f32 v30, v167, v168
	v_cvt_pk_bf16_f32 v31, v169, v170
	ds_read2st64_b64 v[36:39], v115 offset1:16
	ds_read2st64_b64 v[126:129], v116 offset1:16
	s_waitcnt lgkmcnt(1)
	v_mov_b32_e32 v130, v36
	s_waitcnt lgkmcnt(0)
	v_mov_b32_e32 v132, v126
	v_mov_b32_e32 v133, v127
	v_mov_b32_e32 v126, v38
	v_mov_b32_e32 v127, v39
	v_mov_b32_e32 v131, v37
	s_nop 0
	v_mfma_f32_16x16x32_bf16 v[8:11], v[126:129], v[28:31], v[8:11]
	ds_read2st64_b64 v[36:39], v115 offset0:32 offset1:48
	ds_read2st64_b64 v[126:129], v116 offset0:32 offset1:48
	v_mfma_f32_16x16x32_bf16 v[16:19], v[130:133], v[28:31], v[16:19]
	s_waitcnt lgkmcnt(1)
	v_mov_b32_e32 v130, v36
	s_waitcnt lgkmcnt(0)
	v_mov_b32_e32 v132, v126
	v_mov_b32_e32 v133, v127
	v_mov_b32_e32 v126, v38
	v_mov_b32_e32 v127, v39
	v_mov_b32_e32 v131, v37
	s_nop 0
	v_mfma_f32_16x16x32_bf16 v[12:15], v[126:129], v[28:31], v[12:15]
	ds_read2st64_b64 v[36:39], v115 offset0:64 offset1:80
	ds_read2st64_b64 v[126:129], v116 offset0:64 offset1:80
	v_mfma_f32_16x16x32_bf16 v[24:27], v[130:133], v[28:31], v[24:27]
	s_waitcnt lgkmcnt(1)
	v_mov_b32_e32 v130, v36
	s_waitcnt lgkmcnt(0)
	v_mov_b32_e32 v132, v126
	v_mov_b32_e32 v133, v127
	v_mov_b32_e32 v126, v38
	v_mov_b32_e32 v127, v39
	v_mov_b32_e32 v131, v37
	s_nop 0
	v_mfma_f32_16x16x32_bf16 v[20:23], v[126:129], v[28:31], v[20:23]
	ds_read2st64_b64 v[36:39], v115 offset0:96 offset1:112
	ds_read2st64_b64 v[126:129], v116 offset0:96 offset1:112
	v_mfma_f32_16x16x32_bf16 v[32:35], v[130:133], v[28:31], v[32:35]
	s_waitcnt lgkmcnt(1)
	v_mov_b32_e32 v130, v36
	v_mov_b32_e32 v131, v37
	s_waitcnt lgkmcnt(0)
	v_mov_b32_e32 v132, v126
	v_mov_b32_e32 v133, v127
	v_mov_b32_e32 v126, v38
	v_mov_b32_e32 v127, v39
	v_mfma_f32_16x16x32_bf16 v[122:125], v[130:133], v[28:31], v[122:125]
	s_nop 0
	v_mfma_f32_16x16x32_bf16 v[4:7], v[126:129], v[28:31], v[4:7]
	v_cvt_pk_bf16_f32 v28, v171, v172
	v_cvt_pk_bf16_f32 v29, v173, v174
	v_cvt_pk_bf16_f32 v30, v175, v176
	v_cvt_pk_bf16_f32 v31, v177, v178
	ds_read2st64_b64 v[36:39], v117 offset1:16
	ds_read2st64_b64 v[126:129], v118 offset1:16
	s_waitcnt lgkmcnt(1)
	v_mov_b32_e32 v130, v36
	s_waitcnt lgkmcnt(0)
	v_mov_b32_e32 v132, v126
	v_mov_b32_e32 v133, v127
	v_mov_b32_e32 v126, v38
	v_mov_b32_e32 v127, v39
	v_mov_b32_e32 v131, v37
	s_nop 0
	v_mfma_f32_16x16x32_bf16 v[8:11], v[126:129], v[28:31], v[8:11]
	ds_read2st64_b64 v[36:39], v117 offset0:32 offset1:48
	ds_read2st64_b64 v[126:129], v118 offset0:32 offset1:48
	v_mfma_f32_16x16x32_bf16 v[16:19], v[130:133], v[28:31], v[16:19]
	s_waitcnt lgkmcnt(1)
	v_mov_b32_e32 v130, v36
	v_mov_b32_e32 v131, v37
	s_waitcnt lgkmcnt(0)
	v_mov_b32_e32 v132, v126
	v_mov_b32_e32 v133, v127
	v_mov_b32_e32 v126, v38
	v_mov_b32_e32 v127, v39
	v_mfma_f32_16x16x32_bf16 v[130:133], v[130:133], v[28:31], v[24:27]
	s_nop 2
	ds_read2st64_b64 v[24:27], v117 offset0:64 offset1:80
	ds_read2st64_b64 v[36:39], v118 offset0:64 offset1:80
	v_mfma_f32_16x16x32_bf16 v[12:15], v[126:129], v[28:31], v[12:15]
	s_waitcnt lgkmcnt(1)
	v_mov_b32_e32 v126, v24
	s_waitcnt lgkmcnt(0)
	v_mov_b32_e32 v128, v36
	v_mov_b32_e32 v129, v37
	v_mov_b32_e32 v36, v26
	v_mov_b32_e32 v37, v27
	v_mov_b32_e32 v127, v25
	s_nop 0
	v_mfma_f32_16x16x32_bf16 v[36:39], v[36:39], v[28:31], v[20:23]
	s_nop 2
	ds_read2st64_b64 v[20:23], v117 offset0:96 offset1:112
	ds_read2st64_b64 v[24:27], v118 offset0:96 offset1:112
	v_cvt_pk_bf16_f32 v134, v179, v180
	v_cvt_pk_bf16_f32 v135, v181, v182
	v_mfma_f32_16x16x32_bf16 v[126:129], v[126:129], v[28:31], v[32:35]
	v_cvt_pk_bf16_f32 v136, v183, v184
	v_cvt_pk_bf16_f32 v137, v185, v51
	s_waitcnt lgkmcnt(0)
	s_nop 1
	v_mov_b32_e32 v34, v24
	v_mov_b32_e32 v35, v25
	v_mov_b32_e32 v24, v22
	v_mov_b32_e32 v25, v23
	v_mov_b32_e32 v32, v20
	v_mov_b32_e32 v33, v21
	v_mfma_f32_16x16x32_bf16 v[4:7], v[24:27], v[28:31], v[4:7]
	ds_read2st64_b64 v[20:23], v119 offset1:16
	ds_read2st64_b64 v[24:27], v120 offset1:16
	v_mfma_f32_16x16x32_bf16 v[122:125], v[32:35], v[28:31], v[122:125]
	s_waitcnt lgkmcnt(1)
	v_mov_b32_e32 v28, v20
	v_mov_b32_e32 v29, v21
	s_waitcnt lgkmcnt(0)
	v_mov_b32_e32 v30, v24
	v_mov_b32_e32 v31, v25
	v_mov_b32_e32 v24, v22
	v_mov_b32_e32 v25, v23
	v_mfma_f32_16x16x32_bf16 v[32:35], v[28:31], v[134:137], v[16:19]
	s_nop 0
	v_mfma_f32_16x16x32_bf16 v[24:27], v[24:27], v[134:137], v[8:11]
	s_nop 2
	ds_read2st64_b64 v[8:11], v119 offset0:32 offset1:48
	ds_read2st64_b64 v[16:19], v120 offset0:32 offset1:48
	s_waitcnt lgkmcnt(1)
	v_mov_b32_e32 v20, v8
	s_waitcnt lgkmcnt(0)
	v_mov_b32_e32 v22, v16
	v_mov_b32_e32 v23, v17
	v_mov_b32_e32 v16, v10
	v_mov_b32_e32 v17, v11
	v_mov_b32_e32 v21, v9
	s_nop 0
	v_mfma_f32_16x16x32_bf16 v[16:19], v[16:19], v[134:137], v[12:15]
	ds_read2st64_b64 v[8:11], v119 offset0:64 offset1:80
	s_nop 1
	ds_read2st64_b64 v[12:15], v120 offset0:64 offset1:80
	v_mfma_f32_16x16x32_bf16 v[28:31], v[20:23], v[134:137], v[130:133]
	s_waitcnt lgkmcnt(1)
	v_mov_b32_e32 v20, v8
	v_mov_b32_e32 v21, v9
	s_waitcnt lgkmcnt(0)
	v_mov_b32_e32 v22, v12
	v_mov_b32_e32 v23, v13
	v_mov_b32_e32 v12, v10
	v_mov_b32_e32 v13, v11
	v_mfma_f32_16x16x32_bf16 v[20:23], v[20:23], v[134:137], v[126:129]
	s_nop 0
	v_mfma_f32_16x16x32_bf16 v[8:11], v[12:15], v[134:137], v[36:39]
	s_nop 2
	ds_read2st64_b64 v[36:39], v119 offset0:96 offset1:112
	ds_read2st64_b64 v[126:129], v120 offset0:96 offset1:112
	s_waitcnt lgkmcnt(1)
	v_mov_b32_e32 v12, v36
	v_div_scale_f32 v36, s[2:3], v186, v186, 1.0
	v_mov_b32_e32 v13, v37
	v_rcp_f32_e32 v37, v36
	s_waitcnt lgkmcnt(0)
	v_mov_b32_e32 v14, v126
	v_mov_b32_e32 v126, v38
	v_mov_b32_e32 v15, v127
	v_fma_f32 v38, -v36, v37, 1.0
	v_fmac_f32_e32 v37, v38, v37
	v_div_scale_f32 v38, vcc, 1.0, v186, 1.0
	v_mov_b32_e32 v127, v39
	v_mul_f32_e32 v39, v38, v37
	v_fma_f32 v51, -v36, v39, v38
	v_fmac_f32_e32 v39, v51, v37
	v_fma_f32 v36, -v36, v39, v38
	v_div_fmas_f32 v36, v36, v37, v39
	v_div_fixup_f32 v38, v36, v186, 1.0
	v_lshlrev_b64 v[36:37], 11, v[80:81]
	v_sub_co_u32_e32 v36, vcc, 0, v36
	v_mov_b32_e32 v51, v3
	s_nop 0
	v_subb_co_u32_e32 v37, vcc, 0, v37, vcc
	v_lshl_add_u64 v[36:37], v[82:83], 0, v[36:37]
	v_lshl_add_u64 v[36:37], v[36:37], 0, s[46:47]
	v_mul_f32_e32 v32, v38, v32
	v_mul_f32_e32 v33, v38, v33
	v_lshl_add_u64 v[36:37], v[36:37], 0, v[50:51]
	v_cvt_pk_bf16_f32 v32, v32, v33
	v_mul_f32_e32 v33, v38, v34
	v_mul_f32_e32 v34, v38, v35
	v_cvt_pk_bf16_f32 v33, v33, v34
	v_add_co_u32_e32 v34, vcc, s90, v36
	v_mul_f32_e32 v24, v38, v24
	s_nop 0
	v_addc_co_u32_e32 v35, vcc, 0, v37, vcc
	v_mul_f32_e32 v25, v38, v25
	s_mov_b64 s[2:3], 0x40e00c00
	global_store_dwordx2 v[34:35], v[32:33], off offset:3072
	v_cvt_pk_bf16_f32 v24, v24, v25
	v_mul_f32_e32 v25, v38, v26
	v_lshl_add_u64 v[80:81], v[36:37], 0, s[2:3]
	v_mul_f32_e32 v26, v38, v27
	v_cvt_pk_bf16_f32 v25, v25, v26
	global_store_dwordx2 v[80:81], v[24:25], off offset:32
	v_mul_f32_e32 v24, v38, v28
	v_mul_f32_e32 v25, v38, v29
	v_cvt_pk_bf16_f32 v24, v24, v25
	v_mul_f32_e32 v25, v38, v30
	v_mul_f32_e32 v16, v38, v16
	v_mul_f32_e32 v17, v38, v17
	v_mul_f32_e32 v26, v38, v31
	v_cvt_pk_bf16_f32 v25, v25, v26
	global_store_dwordx2 v[80:81], v[24:25], off offset:64
	v_cvt_pk_bf16_f32 v16, v16, v17
	v_mul_f32_e32 v17, v38, v18
	v_mul_f32_e32 v18, v38, v19
	v_cvt_pk_bf16_f32 v17, v17, v18
	v_mfma_f32_16x16x32_bf16 v[12:15], v[12:15], v[134:137], v[122:125]
	global_store_dwordx2 v[80:81], v[16:17], off offset:96
	v_mul_f32_e32 v16, v38, v20
	v_mul_f32_e32 v17, v38, v21
	v_mfma_f32_16x16x32_bf16 v[4:7], v[126:129], v[134:137], v[4:7]
	v_cvt_pk_bf16_f32 v16, v16, v17
	v_mul_f32_e32 v17, v38, v22
	v_mul_f32_e32 v8, v38, v8
	v_mul_f32_e32 v9, v38, v9
	v_mul_f32_e32 v18, v38, v23
	v_cvt_pk_bf16_f32 v17, v17, v18
	global_store_dwordx2 v[80:81], v[16:17], off offset:128
	v_cvt_pk_bf16_f32 v8, v8, v9
	v_mul_f32_e32 v9, v38, v10
	v_mul_f32_e32 v10, v38, v11
	v_cvt_pk_bf16_f32 v9, v9, v10
	global_store_dwordx2 v[80:81], v[8:9], off offset:160
	v_mul_f32_e32 v8, v38, v12
	v_mul_f32_e32 v9, v38, v13
	v_cvt_pk_bf16_f32 v8, v8, v9
	v_mul_f32_e32 v9, v38, v14
	v_mul_f32_e32 v4, v38, v4
	v_mul_f32_e32 v5, v38, v5
	v_mul_f32_e32 v10, v38, v15
	v_cvt_pk_bf16_f32 v9, v9, v10
	global_store_dwordx2 v[80:81], v[8:9], off offset:192
	v_cvt_pk_bf16_f32 v4, v4, v5
	v_mul_f32_e32 v5, v38, v6
	v_mul_f32_e32 v6, v38, v7
	v_cvt_pk_bf16_f32 v5, v5, v6
	global_store_dwordx2 v[80:81], v[4:5], off offset:224
	s_barrier
	s_cbranch_scc0 .LBB0_839
